# speedup vs baseline: 1.0009x; 1.0009x over previous
.Lg1_seam:
	s_sleep 20
	s_branch .LBB1_54
	s_nop 0
	s_nop 0
	s_nop 0
	s_nop 0
	s_nop 0
	s_nop 0
	s_nop 0
	s_nop 0
	s_nop 0
	s_nop 0
	s_nop 0
	s_nop 0
	s_nop 0
	s_nop 0
	s_nop 0
	s_nop 0
	s_nop 0
	s_nop 0
	s_nop 0
	s_nop 0
	s_nop 0
	s_nop 0
	s_nop 0
	s_nop 0
	s_nop 0
	s_nop 0
	s_nop 0
	s_nop 0
	s_nop 0
	s_endpgm
